# speedup vs baseline: 1.0064x; 1.0064x over previous
.LBB0_16:
	s_or_b64 exec, exec, s[10:11]
	v_mul_f32_dpp v46, v46, v46 quad_perm:[1,0,3,2] row_mask:0xf bank_mask:0xf bound_ctrl:1
	s_mov_b32 s18, 0
	s_mov_b64 s[10:11], -1
	v_mul_f32_dpp v46, v46, v46 quad_perm:[2,3,0,1] row_mask:0xf bank_mask:0xf bound_ctrl:1
	s_waitcnt lgkmcnt(0)
	s_nop 1
	v_mul_f32_dpp v46, v46, v46 row_half_mirror row_mask:0xf bank_mask:0xf bound_ctrl:1
	s_nop 1
	v_mul_f32_dpp v46, v46, v46 row_ror:8 row_mask:0xf bank_mask:0xf bound_ctrl:1
	v_mov_b32_e32 v47, v46
	s_nop 1
	v_permlane16_swap_b32 v47, v46
	s_waitcnt lgkmcnt(0)
	v_mul_f32_e32 v46, v46, v47
	ds_bpermute_b32 v47, v19, v46

.LBB0_23:
	s_or_b64 exec, exec, s[8:9]
	v_mul_f32_dpp v53, v53, v53 quad_perm:[1,0,3,2] row_mask:0xf bank_mask:0xf bound_ctrl:1
	s_mov_b32 s14, 0
	s_mov_b64 s[8:9], -1
	v_mul_f32_dpp v53, v53, v53 quad_perm:[2,3,0,1] row_mask:0xf bank_mask:0xf bound_ctrl:1
	v_mov_b32_e32 v64, 0
	v_mov_b32_e32 v69, 0
	v_mov_b32_e32 v70, 0
	v_mov_b32_e32 v58, 0
	s_waitcnt lgkmcnt(0)
	s_nop 1
	v_mul_f32_dpp v53, v53, v53 row_half_mirror row_mask:0xf bank_mask:0xf bound_ctrl:1
	v_mov_b32_e32 v59, 0
	v_mov_b32_e32 v62, 0
	v_mul_f32_dpp v53, v53, v53 row_ror:8 row_mask:0xf bank_mask:0xf bound_ctrl:1
	v_mov_b32_e32 v54, v53
	s_nop 1
	v_permlane16_swap_b32 v54, v53
	v_mov_b32_e32 v63, 0
	v_mov_b32_e32 v56, v47
	v_mov_b32_e32 v57, v46
	v_mov_b32_e32 v60, v45
	s_waitcnt lgkmcnt(0)
	v_mul_f32_e32 v53, v53, v54
	ds_bpermute_b32 v54, v19, v53
	v_mov_b32_e32 v61, v5
	v_mov_b32_e32 v65, v51
	v_mov_b32_e32 v66, v50
	v_mov_b32_e32 v67, v49
	v_mov_b32_e32 v68, v48
.LBB0_24:
	s_lshl_b32 s10, s14, 4
	s_lshl_b32 s11, s14, 6
	v_cndmask_b32_e64 v71, 0, 1, s[8:9]
	s_or_b32 s20, s10, 1
	v_or_b32_e32 v73, s11, v36
	v_cmp_ne_u32_e32 vcc, 1, v71
	v_readlane_b32 s28, v4, s10
	v_or_b32_e32 v71, s11, v21
	v_or_b32_e32 v74, s11, v37
	v_readlane_b32 s31, v4, s20
	ds_bpermute_b32 v84, v73, v2
	v_bitop3_b32 v72, s11, 12, v21 bitop3:0x36
	v_or_b32_e32 v75, s11, v38
	v_or_b32_e32 v76, s11, v39
	ds_bpermute_b32 v78, v71, v2 offset:8
	ds_bpermute_b32 v79, v71, v3 offset:8
	ds_bpermute_b32 v80, v71, v4 offset:8
	ds_bpermute_b32 v85, v73, v3
	ds_bpermute_b32 v87, v74, v2
	ds_bpermute_b32 v88, v74, v3
	v_mov_b32_e32 v71, s28
	v_fma_f32 v98, v71, v67, v70
	v_fma_f32 v99, -v71, v68, v69
	v_fma_f32 v100, v71, v65, v64
	v_fma_f32 v101, -v71, v66, v55
	v_mov_b32_e32 v102, s31
	v_fma_f32 v68, v71, v69, v68
	v_fma_f32 v67, -v71, v70, v67
	v_fma_f32 v55, v71, v55, v66
	v_fma_f32 v64, -v71, v64, v65
	v_fma_f32 v107, v102, v60, v63
	v_fma_f32 v109, v102, v56, v59
	v_fma_f32 v110, -v102, v57, v58
	v_fma_f32 v60, -v102, v63, v60
	v_fma_f32 v57, v102, v58, v57
	v_fma_f32 v56, -v102, v59, v56
	ds_bpermute_b32 v58, v19, v67
	ds_bpermute_b32 v59, v19, v68
	ds_bpermute_b32 v63, v19, v55
	s_waitcnt lgkmcnt(4)
	v_mul_f32 v122, v84, v87
	s_waitcnt lgkmcnt(3)
	v_mul_f32 v84, v84, v88
	s_or_b32 s21, s10, 8
	s_or_b32 s15, s10, 9
	v_readlane_b32 s27, v3, s10
	v_or_b32_e32 v77, s11, v40
	ds_bpermute_b32 v81, v72, v2
	ds_bpermute_b32 v83, v72, v4
	ds_bpermute_b32 v92, v75, v2
	ds_bpermute_b32 v93, v75, v3
	ds_bpermute_b32 v94, v76, v2
	ds_bpermute_b32 v95, v76, v3
	v_fma_f32 v108, -v102, v61, v62
	v_fma_f32 v61, v102, v62, v61
	ds_bpermute_b32 v62, v19, v64
	s_waitcnt lgkmcnt(2)
	v_mul_f32 v123, v92, v94
	v_fma_f32 v88, -v85, v88, v122
	v_fma_f32 v84, v85, v87, v84
	v_fma_f32 v63, -v83, v63, v67
	v_fma_f32 v55, v80, v58, v55
	v_fma_f32 v58, -v80, v59, v64
	s_waitcnt lgkmcnt(1)
	v_fma_f32 v85, -v93, v95, v123
	v_mul_f32 v59, v88, v78
	v_mul_f32 v64, v88, v79
	v_mul_f32 v67, v88, v81
	v_readlane_b32 s19, v2, s10
	v_readlane_b32 s29, v2, s20
	v_readlane_b32 s30, v3, s20
	ds_bpermute_b32 v82, v72, v3
	v_mov_b32_e32 v91, s27
	v_readlane_b32 s27, v2, s21
	v_readlane_b32 s28, v2, s15
	v_readlane_b32 s33, v3, s21
	v_readlane_b32 s34, v3, s15
	ds_bpermute_b32 v96, v77, v2
	ds_bpermute_b32 v97, v77, v3
	ds_bpermute_b32 v112, v19, v101
	ds_bpermute_b32 v113, v19, v100
	ds_bpermute_b32 v114, v19, v60
	ds_bpermute_b32 v115, v19, v61
	ds_bpermute_b32 v116, v19, v56
	ds_bpermute_b32 v117, v19, v57
	ds_bpermute_b32 v118, v19, v108
	ds_bpermute_b32 v119, v19, v107
	ds_bpermute_b32 v120, v19, v110
	v_mul_f32 v92, v92, v95
	s_waitcnt lgkmcnt(12)
	v_fma_f32 v62, v83, v62, v68
	s_waitcnt lgkmcnt(11)
	v_mul_f32 v68, v88, v82
	s_waitcnt lgkmcnt(10)
	v_mul_f32 v88, v85, v96
	s_waitcnt lgkmcnt(9)
	v_mul_f32 v85, v85, v97
	v_fma_f32 v59, -v84, v79, v59
	v_fma_f32 v87, v93, v94, v92
	v_fma_f32 v64, v84, v78, v64
	v_fma_f32 v67, -v84, v82, v67
	ds_bpermute_b32 v86, v73, v4
	v_fma_f32 v78, -v87, v97, v88
	v_mov_b32_e32 v90, s19
	v_mov_b32_e32 v65, s29
	v_mov_b32_e32 v66, s30
	v_mov_b32_e32 v103, s27
	v_mov_b32_e32 v104, s33
	v_mov_b32_e32 v105, s28
	v_mov_b32_e32 v106, s34
	ds_bpermute_b32 v102, v19, v99
	ds_bpermute_b32 v111, v19, v98
	ds_bpermute_b32 v121, v19, v109
	s_waitcnt lgkmcnt(12)
	v_fma_f32 v92, v83, v112, v98
	s_waitcnt lgkmcnt(11)
	v_fma_f32 v93, -v83, v113, v99
	s_waitcnt lgkmcnt(2)
	v_fma_f32 v94, v80, v102, v100
	s_waitcnt lgkmcnt(1)
	v_fma_f32 v95, -v80, v111, v101
	v_fma_f32 v98, v83, v120, v107
	s_waitcnt lgkmcnt(0)
	v_fma_f32 v99, -v83, v121, v108
	v_fma_f32 v100, v80, v118, v109
	v_fma_f32 v101, -v80, v119, v110
	v_fma_f32 v61, v83, v116, v61
	v_fma_f32 v60, -v83, v117, v60
	v_fma_f32 v57, v80, v114, v57
	v_fma_f32 v56, -v80, v115, v56
	ds_swizzle_b32 v80, v58 offset:swizzle(BITMASK_PERM,"iippp")
	ds_swizzle_b32 v83, v55 offset:swizzle(BITMASK_PERM,"iippp")
	v_fma_f32 v68, v84, v81, v68
	v_fma_f32 v79, v87, v96, v85
	ds_swizzle_b32 v81, v56 offset:swizzle(BITMASK_PERM,"iippp")
	ds_swizzle_b32 v82, v57 offset:swizzle(BITMASK_PERM,"iippp")
	ds_swizzle_b32 v84, v60 offset:swizzle(BITMASK_PERM,"iippp")
	ds_swizzle_b32 v85, v61 offset:swizzle(BITMASK_PERM,"iippp")
	ds_swizzle_b32 v87, v101 offset:swizzle(BITMASK_PERM,"iippp")
	ds_swizzle_b32 v88, v100 offset:swizzle(BITMASK_PERM,"iippp")
	v_mul_f32 v112, v59, v90
	v_mul_f32 v113, v59, v91
	v_mul_f32 v114, v59, v65
	v_mul_f32 v59, v59, v66
	v_mul_f32 v115, v67, v90
	v_mul_f32 v116, v67, v91
	v_mul_f32 v117, v67, v65
	v_mul_f32 v67, v67, v66
	v_mul_f32 v118, v78, v103
	v_mul_f32 v119, v78, v104
	v_mul_f32 v120, v78, v105
	v_mul_f32 v78, v78, v106
	ds_swizzle_b32 v102, v63 offset:swizzle(BITMASK_PERM,"iippp")
	ds_swizzle_b32 v107, v62 offset:swizzle(BITMASK_PERM,"iippp")
	ds_swizzle_b32 v108, v95 offset:swizzle(BITMASK_PERM,"iippp")
	ds_swizzle_b32 v109, v94 offset:swizzle(BITMASK_PERM,"iippp")
	ds_swizzle_b32 v110, v93 offset:swizzle(BITMASK_PERM,"iippp")
	ds_swizzle_b32 v111, v92 offset:swizzle(BITMASK_PERM,"iippp")
	ds_swizzle_b32 v96, v99 offset:swizzle(BITMASK_PERM,"iippp")
	ds_swizzle_b32 v97, v98 offset:swizzle(BITMASK_PERM,"iippp")
	v_fma_f32 v112, -v64, v91, v112
	v_fma_f32 v113, v64, v90, v113
	v_fma_f32 v114, -v64, v66, v114
	v_fma_f32 v59, v64, v65, v59
	v_fma_f32 v64, -v68, v91, v115
	v_fma_f32 v90, v68, v90, v116
	v_fma_f32 v66, -v68, v66, v117
	v_fma_f32 v65, v68, v65, v67
	v_fma_f32 v67, -v79, v104, v118
	v_fma_f32 v68, v79, v103, v119
	v_fma_f32 v91, -v79, v106, v120
	v_fma_f32 v78, v79, v105, v78
	s_waitcnt lgkmcnt(3)
	v_fma_f32 v79, v86, v110, v92
	s_waitcnt lgkmcnt(2)
	v_fma_f32 v92, -v86, v111, v93
	v_fma_f32 v93, v86, v108, v94
	v_fma_f32 v94, -v86, v109, v95
	v_fma_f32 v62, v86, v102, v62
	v_fma_f32 v63, -v86, v107, v63
	v_fma_f32 v55, v86, v80, v55
	v_fma_f32 v58, -v86, v83, v58
	s_waitcnt lgkmcnt(1)
	v_fma_f32 v80, v86, v96, v98
	s_waitcnt lgkmcnt(0)
	v_fma_f32 v83, -v86, v97, v99
	v_fma_f32 v87, v86, v87, v100
	v_fma_f32 v88, -v86, v88, v101
	v_fma_f32 v61, v86, v84, v61
	v_fma_f32 v60, -v86, v85, v60
	v_fma_f32 v57, v86, v81, v57
	v_fma_f32 v56, -v86, v82, v56
	ds_swizzle_b32 v81, v58 offset:swizzle(BITMASK_PERM,"ppiip")
	ds_swizzle_b32 v82, v55 offset:swizzle(BITMASK_PERM,"ppiip")
	ds_swizzle_b32 v84, v63 offset:swizzle(BITMASK_PERM,"ppiip")
	ds_swizzle_b32 v85, v62 offset:swizzle(BITMASK_PERM,"ppiip")
	ds_swizzle_b32 v86, v94 offset:swizzle(BITMASK_PERM,"ppiip")
	ds_swizzle_b32 v95, v93 offset:swizzle(BITMASK_PERM,"ppiip")
	ds_bpermute_b32 v89, v74, v4
	v_readlane_b32 s35, v4, s21
	v_readlane_b32 s36, v4, s15
	ds_swizzle_b32 v96, v92 offset:swizzle(BITMASK_PERM,"ppiip")
	ds_swizzle_b32 v97, v79 offset:swizzle(BITMASK_PERM,"ppiip")
	ds_swizzle_b32 v98, v56 offset:swizzle(BITMASK_PERM,"ppiip")
	ds_swizzle_b32 v99, v57 offset:swizzle(BITMASK_PERM,"ppiip")
	ds_swizzle_b32 v100, v60 offset:swizzle(BITMASK_PERM,"ppiip")
	ds_swizzle_b32 v101, v61 offset:swizzle(BITMASK_PERM,"ppiip")
	ds_swizzle_b32 v102, v88 offset:swizzle(BITMASK_PERM,"ppiip")
	ds_swizzle_b32 v103, v87 offset:swizzle(BITMASK_PERM,"ppiip")
	ds_swizzle_b32 v104, v83 offset:swizzle(BITMASK_PERM,"ppiip")
	ds_swizzle_b32 v105, v80 offset:swizzle(BITMASK_PERM,"ppiip")
	s_waitcnt lgkmcnt(9)
	v_fma_f32 v79, v89, v96, v79
	s_waitcnt lgkmcnt(8)
	v_fma_f32 v92, -v89, v97, v92
	v_fma_f32 v86, v89, v86, v93
	v_fma_f32 v93, -v89, v95, v94
	v_fma_f32 v62, v89, v84, v62
	v_fma_f32 v63, -v89, v85, v63
	v_fma_f32 v55, v89, v81, v55
	v_fma_f32 v58, -v89, v82, v58
	s_waitcnt lgkmcnt(1)
	v_fma_f32 v80, v89, v104, v80
	s_waitcnt lgkmcnt(0)
	v_fma_f32 v81, -v89, v105, v83
	v_fma_f32 v82, v89, v102, v87
	v_fma_f32 v83, -v89, v103, v88
	v_fma_f32 v61, v89, v100, v61
	v_fma_f32 v60, -v89, v101, v60
	v_fma_f32 v57, v89, v98, v57
	v_fma_f32 v56, -v89, v99, v56
	v_mul_f32 v84, v112, v58
	v_mul_f32 v85, v112, v55
	v_mul_f32 v87, v64, v63
	v_mul_f32 v88, v64, v62
	v_mul_f32 v95, v64, v92
	v_mul_f32 v64, v64, v79
	v_mov_b32_e32 v69, s35
	v_mov_b32_e32 v70, s36
	v_mul_f32 v89, v112, v93
	v_mul_f32 v94, v112, v86
	v_fma_f32 v55, -v113, v55, v84
	v_fma_f32 v58, v113, v58, v85
	v_fma_f32 v62, -v90, v62, v87
	v_fma_f32 v63, v90, v63, v88
	v_mul_f32 v84, v114, v56
	v_mul_f32 v85, v114, v57
	v_mul_f32 v87, v66, v60
	v_mul_f32 v88, v66, v61
	v_mul_f32 v96, v114, v83
	v_mul_f32 v97, v114, v82
	v_mul_f32 v98, v66, v81
	v_mul_f32 v66, v66, v80
	v_fma_f32 v86, -v113, v86, v89
	v_fma_f32 v79, -v90, v79, v95
	v_fma_f32 v64, v90, v92, v64
	v_fma_f32 v57, -v59, v57, v84
	v_fma_f32 v56, v59, v56, v85
	v_fma_f32 v61, -v65, v61, v87
	v_fma_f32 v60, v65, v60, v88
	v_fma_f32 v82, -v59, v82, v96
	v_fma_f32 v59, v59, v83, v97
	v_fma_f32 v80, -v65, v80, v98
	v_fma_f32 v65, v65, v81, v66
	ds_bpermute_b32 v75, v75, v4
	v_fma_f32 v89, v113, v93, v94
	v_fma_f32 v66, v69, v82, v64
	v_fma_f32 v81, -v69, v59, v79
	v_fma_f32 v84, -v70, v65, v86
	v_fma_f32 v65, v70, v86, v65
	v_fma_f32 v59, v69, v79, v59
	v_fma_f32 v83, v70, v80, v89
	v_fma_f32 v80, -v70, v89, v80
	v_fma_f32 v64, -v69, v64, v82
	v_fma_f32 v79, v69, v55, v60
	v_fma_f32 v82, -v69, v58, v61
	v_fma_f32 v85, v70, v62, v56
	v_fma_f32 v86, -v70, v63, v57
	v_fma_f32 v57, v70, v57, v63
	v_fma_f32 v56, -v70, v56, v62
	v_fma_f32 v58, v69, v61, v58
	v_fma_f32 v55, -v69, v60, v55
	ds_bpermute_b32 v60, v20, v55
	ds_bpermute_b32 v61, v20, v58
	ds_bpermute_b32 v62, v20, v56
	ds_bpermute_b32 v63, v20, v57
	ds_bpermute_b32 v69, v20, v86
	ds_bpermute_b32 v70, v20, v85
	ds_bpermute_b32 v87, v20, v82
	ds_bpermute_b32 v92, v20, v80
	ds_bpermute_b32 v88, v20, v79
	ds_bpermute_b32 v89, v20, v64
	ds_bpermute_b32 v90, v20, v59
	ds_bpermute_b32 v93, v20, v81
	ds_bpermute_b32 v94, v20, v66
	ds_bpermute_b32 v95, v20, v84
	ds_bpermute_b32 v96, v20, v83
	ds_bpermute_b32 v97, v20, v65
	s_waitcnt lgkmcnt(4)
	v_fma_f32 v66, v75, v93, v66
	s_waitcnt lgkmcnt(3)
	v_fma_f32 v81, -v75, v94, v81
	s_waitcnt lgkmcnt(2)
	v_fma_f32 v83, v75, v95, v83
	s_waitcnt lgkmcnt(1)
	v_fma_f32 v84, -v75, v96, v84
	v_fma_f32 v65, v75, v92, v65
	s_waitcnt lgkmcnt(0)
	v_fma_f32 v80, -v75, v97, v80
	v_fma_f32 v59, v75, v89, v59
	v_fma_f32 v64, -v75, v90, v64
	v_fma_f32 v79, v75, v87, v79
	v_fma_f32 v82, -v75, v88, v82
	v_fma_f32 v69, v75, v69, v85
	v_fma_f32 v70, -v75, v70, v86
	v_fma_f32 v57, v75, v62, v57
	v_fma_f32 v56, -v75, v63, v56
	v_fma_f32 v58, v75, v60, v58
	v_fma_f32 v55, -v75, v61, v55
	ds_swizzle_b32 v60, v55 offset:swizzle(BITMASK_PERM,"piipp")
	ds_swizzle_b32 v61, v58 offset:swizzle(BITMASK_PERM,"piipp")
	ds_swizzle_b32 v62, v56 offset:swizzle(BITMASK_PERM,"piipp")
	ds_swizzle_b32 v63, v57 offset:swizzle(BITMASK_PERM,"piipp")
	ds_swizzle_b32 v75, v70 offset:swizzle(BITMASK_PERM,"piipp")
	ds_swizzle_b32 v85, v69 offset:swizzle(BITMASK_PERM,"piipp")
	ds_swizzle_b32 v86, v82 offset:swizzle(BITMASK_PERM,"piipp")
	ds_swizzle_b32 v87, v79 offset:swizzle(BITMASK_PERM,"piipp")
	ds_swizzle_b32 v92, v81 offset:swizzle(BITMASK_PERM,"piipp")
	ds_bpermute_b32 v76, v76, v4
	ds_swizzle_b32 v88, v64 offset:swizzle(BITMASK_PERM,"piipp")
	ds_swizzle_b32 v89, v59 offset:swizzle(BITMASK_PERM,"piipp")
	ds_swizzle_b32 v90, v80 offset:swizzle(BITMASK_PERM,"piipp")
	ds_swizzle_b32 v93, v66 offset:swizzle(BITMASK_PERM,"piipp")
	ds_swizzle_b32 v94, v84 offset:swizzle(BITMASK_PERM,"piipp")
	ds_swizzle_b32 v95, v83 offset:swizzle(BITMASK_PERM,"piipp")
	ds_bpermute_b32 v77, v77, v4
	ds_swizzle_b32 v96, v65 offset:swizzle(BITMASK_PERM,"piipp")
	s_waitcnt lgkmcnt(8)
	v_fma_f32 v66, v76, v92, v66
	s_waitcnt lgkmcnt(4)
	v_fma_f32 v81, -v76, v93, v81
	s_waitcnt lgkmcnt(3)
	v_fma_f32 v83, v76, v94, v83
	s_waitcnt lgkmcnt(2)
	v_fma_f32 v84, -v76, v95, v84
	v_fma_f32 v65, v76, v90, v65
	s_waitcnt lgkmcnt(0)
	v_fma_f32 v80, -v76, v96, v80
	v_fma_f32 v59, v76, v88, v59
	v_fma_f32 v64, -v76, v89, v64
	v_fma_f32 v79, v76, v86, v79
	v_fma_f32 v82, -v76, v87, v82
	v_fma_f32 v69, v76, v75, v69
	v_fma_f32 v70, -v76, v85, v70
	v_fma_f32 v57, v76, v62, v57
	v_fma_f32 v56, -v76, v63, v56
	v_fma_f32 v58, v76, v60, v58
	v_fma_f32 v55, -v76, v61, v55
	s_nop 1
	v_mov_b32_dpp v85, v82 quad_perm:[3,2,1,0] row_mask:0xf bank_mask:0xf bound_ctrl:1
	v_mov_b32_dpp v75, v70 quad_perm:[3,2,1,0] row_mask:0xf bank_mask:0xf bound_ctrl:1
	v_mov_b32_dpp v60, v55 quad_perm:[3,2,1,0] row_mask:0xf bank_mask:0xf bound_ctrl:1
	v_mov_b32_dpp v61, v58 quad_perm:[3,2,1,0] row_mask:0xf bank_mask:0xf bound_ctrl:1
	v_mov_b32_dpp v62, v56 quad_perm:[3,2,1,0] row_mask:0xf bank_mask:0xf bound_ctrl:1
	v_mov_b32_dpp v63, v57 quad_perm:[3,2,1,0] row_mask:0xf bank_mask:0xf bound_ctrl:1
	v_mov_b32_dpp v86, v79 quad_perm:[3,2,1,0] row_mask:0xf bank_mask:0xf bound_ctrl:1
	v_mov_b32_dpp v87, v64 quad_perm:[3,2,1,0] row_mask:0xf bank_mask:0xf bound_ctrl:1
	v_mov_b32_dpp v92, v84 quad_perm:[3,2,1,0] row_mask:0xf bank_mask:0xf bound_ctrl:1
	v_mov_b32_dpp v76, v69 quad_perm:[3,2,1,0] row_mask:0xf bank_mask:0xf bound_ctrl:1
	v_mov_b32_dpp v88, v59 quad_perm:[3,2,1,0] row_mask:0xf bank_mask:0xf bound_ctrl:1
	v_mov_b32_dpp v89, v80 quad_perm:[3,2,1,0] row_mask:0xf bank_mask:0xf bound_ctrl:1
	v_mov_b32_dpp v90, v65 quad_perm:[3,2,1,0] row_mask:0xf bank_mask:0xf bound_ctrl:1
	v_mov_b32_dpp v93, v83 quad_perm:[3,2,1,0] row_mask:0xf bank_mask:0xf bound_ctrl:1
	v_mov_b32_dpp v94, v81 quad_perm:[3,2,1,0] row_mask:0xf bank_mask:0xf bound_ctrl:1
	v_mov_b32_dpp v95, v66 quad_perm:[3,2,1,0] row_mask:0xf bank_mask:0xf bound_ctrl:1
	v_fma_f32 v66, v77, v94, v66
	v_fma_f32 v81, -v77, v95, v81
	v_fma_f32 v83, v77, v92, v83
	v_fma_f32 v84, -v77, v93, v84
	v_fma_f32 v65, v77, v89, v65
	v_fma_f32 v80, -v77, v90, v80
	v_fma_f32 v59, v77, v87, v59
	v_fma_f32 v64, -v77, v88, v64
	v_fma_f32 v79, v77, v85, v79
	v_fma_f32 v82, -v77, v86, v82
	v_fma_f32 v69, v77, v75, v69
	v_fma_f32 v70, -v77, v76, v70
	v_fma_f32 v57, v77, v62, v57
	v_fma_f32 v56, -v77, v63, v56
	v_fma_f32 v58, v77, v60, v58
	v_fma_f32 v55, -v77, v61, v55
	v_mul_f32 v77, v67, v82
	v_mul_f32 v75, v91, v70
	v_mul_f32 v63, v91, v57
	v_mul_f32 v62, v91, v56
	v_mul_f32 v61, v67, v58
	v_mul_f32 v60, v67, v55
	v_mul_f32 v85, v67, v79
	v_mul_f32 v86, v67, v64
	v_mul_f32 v87, v67, v59
	v_mul_f32 v92, v67, v81
	v_mul_f32 v67, v67, v66
	v_mul_f32 v76, v91, v69
	v_mul_f32 v88, v91, v80
	v_mul_f32 v89, v91, v65
	v_mul_f32 v90, v91, v84
	v_mul_f32 v91, v91, v83
	v_fma_f32 v58, -v68, v58, v60
	v_fma_f32 v55, v68, v55, v61
	v_fma_f32 v57, -v78, v57, v62
	v_fma_f32 v56, v78, v56, v63
	v_fma_f32 v60, -v78, v69, v75
	v_fma_f32 v61, v78, v70, v76
	v_fma_f32 v62, -v68, v79, v77
	v_fma_f32 v63, v68, v82, v85
	v_fma_f32 v59, -v68, v59, v86
	v_fma_f32 v64, v68, v64, v87
	v_fma_f32 v65, -v78, v65, v88
	v_fma_f32 v69, v78, v80, v89
	v_fma_f32 v70, -v78, v83, v90
	v_fma_f32 v75, v78, v84, v91
	v_fma_f32 v66, -v68, v66, v92
	v_fma_f32 v67, v68, v81, v67
	s_nop 0
	s_nop 1
	v_fmac_f32_dpp v58, v58, v23 quad_perm:[1,0,3,2] row_mask:0xf bank_mask:0xf
	v_fmac_f32_dpp v57, v57, v23 quad_perm:[1,0,3,2] row_mask:0xf bank_mask:0xf
	v_fmac_f32_dpp v60, v60, v23 quad_perm:[1,0,3,2] row_mask:0xf bank_mask:0xf
	v_fmac_f32_dpp v62, v62, v23 quad_perm:[1,0,3,2] row_mask:0xf bank_mask:0xf
	v_fmac_f32_dpp v55, v55, v23 quad_perm:[1,0,3,2] row_mask:0xf bank_mask:0xf
	v_fmac_f32_dpp v56, v56, v23 quad_perm:[1,0,3,2] row_mask:0xf bank_mask:0xf
	v_fmac_f32_dpp v61, v61, v23 quad_perm:[1,0,3,2] row_mask:0xf bank_mask:0xf
	v_fmac_f32_dpp v63, v63, v23 quad_perm:[1,0,3,2] row_mask:0xf bank_mask:0xf

	s_or_b32 s18, s10, 4
	v_fmac_f32_dpp v59, v59, v23 quad_perm:[1,0,3,2] row_mask:0xf bank_mask:0xf
	v_fmac_f32_dpp v65, v65, v23 quad_perm:[1,0,3,2] row_mask:0xf bank_mask:0xf
	v_fmac_f32_dpp v70, v70, v23 quad_perm:[1,0,3,2] row_mask:0xf bank_mask:0xf
	v_fmac_f32_dpp v66, v66, v23 quad_perm:[1,0,3,2] row_mask:0xf bank_mask:0xf
	v_fmac_f32_dpp v64, v64, v23 quad_perm:[1,0,3,2] row_mask:0xf bank_mask:0xf
	v_fmac_f32_dpp v69, v69, v23 quad_perm:[1,0,3,2] row_mask:0xf bank_mask:0xf
	v_fmac_f32_dpp v75, v75, v23 quad_perm:[1,0,3,2] row_mask:0xf bank_mask:0xf
	v_fmac_f32_dpp v67, v67, v23 quad_perm:[1,0,3,2] row_mask:0xf bank_mask:0xf

	v_fmac_f32_dpp v58, v58, v24 quad_perm:[2,3,0,1] row_mask:0xf bank_mask:0xf
	v_fmac_f32_dpp v57, v57, v24 quad_perm:[2,3,0,1] row_mask:0xf bank_mask:0xf
	v_fmac_f32_dpp v60, v60, v24 quad_perm:[2,3,0,1] row_mask:0xf bank_mask:0xf
	v_fmac_f32_dpp v62, v62, v24 quad_perm:[2,3,0,1] row_mask:0xf bank_mask:0xf
	v_fmac_f32_dpp v55, v55, v24 quad_perm:[2,3,0,1] row_mask:0xf bank_mask:0xf
	v_fmac_f32_dpp v56, v56, v24 quad_perm:[2,3,0,1] row_mask:0xf bank_mask:0xf
	v_fmac_f32_dpp v61, v61, v24 quad_perm:[2,3,0,1] row_mask:0xf bank_mask:0xf
	v_fmac_f32_dpp v63, v63, v24 quad_perm:[2,3,0,1] row_mask:0xf bank_mask:0xf

	s_or_b32 s22, s10, 3
	v_fmac_f32_dpp v59, v59, v24 quad_perm:[2,3,0,1] row_mask:0xf bank_mask:0xf
	v_fmac_f32_dpp v65, v65, v24 quad_perm:[2,3,0,1] row_mask:0xf bank_mask:0xf
	v_fmac_f32_dpp v70, v70, v24 quad_perm:[2,3,0,1] row_mask:0xf bank_mask:0xf
	v_fmac_f32_dpp v66, v66, v24 quad_perm:[2,3,0,1] row_mask:0xf bank_mask:0xf
	v_fmac_f32_dpp v64, v64, v24 quad_perm:[2,3,0,1] row_mask:0xf bank_mask:0xf
	v_fmac_f32_dpp v69, v69, v24 quad_perm:[2,3,0,1] row_mask:0xf bank_mask:0xf
	v_fmac_f32_dpp v75, v75, v24 quad_perm:[2,3,0,1] row_mask:0xf bank_mask:0xf
	v_fmac_f32_dpp v67, v67, v24 quad_perm:[2,3,0,1] row_mask:0xf bank_mask:0xf

	v_readlane_b32 s19, v52, s18
	v_mov_b32_dpp v68, v58 row_half_mirror row_mask:0xf bank_mask:0xf bound_ctrl:1
	v_mov_b32_dpp v76, v57 row_half_mirror row_mask:0xf bank_mask:0xf bound_ctrl:1
	v_mov_b32_dpp v77, v60 row_half_mirror row_mask:0xf bank_mask:0xf bound_ctrl:1
	v_mov_b32_dpp v78, v62 row_half_mirror row_mask:0xf bank_mask:0xf bound_ctrl:1
	v_mov_b32_dpp v79, v55 row_half_mirror row_mask:0xf bank_mask:0xf bound_ctrl:1
	v_mov_b32_dpp v80, v56 row_half_mirror row_mask:0xf bank_mask:0xf bound_ctrl:1
	v_mov_b32_dpp v81, v61 row_half_mirror row_mask:0xf bank_mask:0xf bound_ctrl:1
	v_mov_b32_dpp v82, v63 row_half_mirror row_mask:0xf bank_mask:0xf bound_ctrl:1
	v_mov_b32_dpp v83, v59 row_half_mirror row_mask:0xf bank_mask:0xf bound_ctrl:1
	v_mov_b32_dpp v84, v65 row_half_mirror row_mask:0xf bank_mask:0xf bound_ctrl:1
	v_mov_b32_dpp v85, v70 row_half_mirror row_mask:0xf bank_mask:0xf bound_ctrl:1
	v_mov_b32_dpp v86, v66 row_half_mirror row_mask:0xf bank_mask:0xf bound_ctrl:1
	v_mov_b32_dpp v87, v64 row_half_mirror row_mask:0xf bank_mask:0xf bound_ctrl:1
	v_mov_b32_dpp v88, v69 row_half_mirror row_mask:0xf bank_mask:0xf bound_ctrl:1
	v_mov_b32_dpp v89, v75 row_half_mirror row_mask:0xf bank_mask:0xf bound_ctrl:1
	v_mov_b32_dpp v90, v67 row_half_mirror row_mask:0xf bank_mask:0xf bound_ctrl:1
	v_fmac_f32_dpp v58, v68, v25 quad_perm:[3,2,1,0] row_mask:0xf bank_mask:0xf
	v_fmac_f32_dpp v57, v76, v25 quad_perm:[3,2,1,0] row_mask:0xf bank_mask:0xf
	v_fmac_f32_dpp v60, v77, v25 quad_perm:[3,2,1,0] row_mask:0xf bank_mask:0xf
	v_fmac_f32_dpp v62, v78, v25 quad_perm:[3,2,1,0] row_mask:0xf bank_mask:0xf
	v_fmac_f32_dpp v55, v79, v25 quad_perm:[3,2,1,0] row_mask:0xf bank_mask:0xf
	v_fmac_f32_dpp v56, v80, v25 quad_perm:[3,2,1,0] row_mask:0xf bank_mask:0xf
	v_fmac_f32_dpp v61, v81, v25 quad_perm:[3,2,1,0] row_mask:0xf bank_mask:0xf
	v_fmac_f32_dpp v63, v82, v25 quad_perm:[3,2,1,0] row_mask:0xf bank_mask:0xf

	v_fmac_f32_dpp v59, v83, v25 quad_perm:[3,2,1,0] row_mask:0xf bank_mask:0xf
	v_fmac_f32_dpp v65, v84, v25 quad_perm:[3,2,1,0] row_mask:0xf bank_mask:0xf
	v_fmac_f32_dpp v70, v85, v25 quad_perm:[3,2,1,0] row_mask:0xf bank_mask:0xf
	v_fmac_f32_dpp v66, v86, v25 quad_perm:[3,2,1,0] row_mask:0xf bank_mask:0xf
	v_fmac_f32_dpp v64, v87, v25 quad_perm:[3,2,1,0] row_mask:0xf bank_mask:0xf
	v_fmac_f32_dpp v69, v88, v25 quad_perm:[3,2,1,0] row_mask:0xf bank_mask:0xf
	v_fmac_f32_dpp v75, v89, v25 quad_perm:[3,2,1,0] row_mask:0xf bank_mask:0xf
	v_fmac_f32_dpp v67, v90, v25 quad_perm:[3,2,1,0] row_mask:0xf bank_mask:0xf

	v_readlane_b32 s18, v52, s22
	s_nop 1
	v_fmac_f32_dpp v58, v58, v26 row_ror:8 row_mask:0xf bank_mask:0xf
	v_fmac_f32_dpp v57, v57, v26 row_ror:8 row_mask:0xf bank_mask:0xf
	v_fmac_f32_dpp v60, v60, v26 row_ror:8 row_mask:0xf bank_mask:0xf
	v_fmac_f32_dpp v62, v62, v26 row_ror:8 row_mask:0xf bank_mask:0xf
	v_fmac_f32_dpp v55, v55, v26 row_ror:8 row_mask:0xf bank_mask:0xf
	v_fmac_f32_dpp v56, v56, v26 row_ror:8 row_mask:0xf bank_mask:0xf
	v_fmac_f32_dpp v61, v61, v26 row_ror:8 row_mask:0xf bank_mask:0xf
	v_fmac_f32_dpp v63, v63, v26 row_ror:8 row_mask:0xf bank_mask:0xf

	v_fmac_f32_dpp v59, v59, v26 row_ror:8 row_mask:0xf bank_mask:0xf
	v_fmac_f32_dpp v65, v65, v26 row_ror:8 row_mask:0xf bank_mask:0xf
	v_fmac_f32_dpp v70, v70, v26 row_ror:8 row_mask:0xf bank_mask:0xf
	v_fmac_f32_dpp v66, v66, v26 row_ror:8 row_mask:0xf bank_mask:0xf
	v_fmac_f32_dpp v64, v64, v26 row_ror:8 row_mask:0xf bank_mask:0xf
	v_fmac_f32_dpp v69, v69, v26 row_ror:8 row_mask:0xf bank_mask:0xf
	v_fmac_f32_dpp v75, v75, v26 row_ror:8 row_mask:0xf bank_mask:0xf
	v_fmac_f32_dpp v67, v67, v26 row_ror:8 row_mask:0xf bank_mask:0xf

	s_or_b32 s23, s10, 2
	v_add_f32 v68, v58, v57
	v_sub_f32 v57, v58, v57
	v_add_f32 v58, v55, v56
	v_sub_f32 v55, v55, v56
	v_add_f32 v56, v60, v62
	v_sub_f32 v60, v60, v62
	v_add_f32 v62, v61, v63
	v_sub_f32 v61, v61, v63
	v_add_f32 v63, v59, v65
	v_sub_f32 v59, v59, v65
	v_add_f32 v65, v64, v69
	v_sub_f32 v64, v64, v69
	v_add_f32 v69, v70, v66
	v_sub_f32 v66, v70, v66
	v_add_f32 v70, v75, v67
	v_sub_f32 v67, v75, v67
	v_add_f32 v75, v68, v56
	v_sub_f32 v56, v68, v56
	v_add_f32 v68, v58, v62
	v_sub_f32 v58, v58, v62
	v_add_f32 v62, v57, v60
	v_sub_f32 v57, v57, v60
	v_add_f32 v60, v55, v61
	v_sub_f32 v55, v55, v61
	v_add_f32 v61, v63, v69
	v_sub_f32 v63, v63, v69
	v_add_f32 v69, v65, v70
	v_sub_f32 v65, v65, v70
	v_add_f32 v70, v59, v66
	v_sub_f32 v59, v59, v66
	v_add_f32 v66, v64, v67
	v_sub_f32 v64, v64, v67
	v_add_f32 v67, v75, v61
	v_sub_f32 v61, v75, v61
	v_add_f32 v75, v68, v69
	v_sub_f32 v68, v68, v69
	v_add_f32 v69, v62, v70
	v_sub_f32 v62, v62, v70
	v_add_f32 v70, v60, v66
	v_sub_f32 v60, v60, v66
	v_add_f32 v66, v56, v63
	v_sub_f32 v56, v56, v63
	v_add_f32 v63, v58, v65
	v_sub_f32 v58, v58, v65
	v_add_f32 v65, v57, v59
	v_sub_f32 v57, v57, v59
	v_add_f32 v59, v55, v64
	v_sub_f32 v55, v55, v64
	v_readlane_b32 s15, v52, s23
	s_nop 1
	v_permlane16_swap_b32 v67, v69
	v_permlane16_swap_b32 v75, v70
	v_permlane16_swap_b32 v66, v65
	v_permlane16_swap_b32 v63, v59
	v_permlane16_swap_b32 v61, v62
	v_permlane16_swap_b32 v68, v60
	v_permlane16_swap_b32 v56, v57
	v_permlane16_swap_b32 v58, v55
	s_or_b32 s24, s10, 5
	v_permlane32_swap_b32 v67, v66
	v_permlane32_swap_b32 v75, v63
	v_permlane32_swap_b32 v69, v65
	v_permlane32_swap_b32 v70, v59
	v_permlane32_swap_b32 v61, v56
	v_permlane32_swap_b32 v68, v58
	v_permlane32_swap_b32 v62, v57
	v_permlane32_swap_b32 v60, v55
	v_readlane_b32 s11, v52, s20
	v_add_f32 v64, v67, v69
	v_sub_f32 v67, v67, v69
	v_add_f32 v69, v75, v70
	v_sub_f32 v70, v75, v70
	v_add_f32 v75, v66, v65
	v_sub_f32 v65, v66, v65
	v_add_f32 v66, v63, v59
	v_sub_f32 v59, v63, v59
	v_add_f32 v63, v61, v62
	v_sub_f32 v61, v61, v62
	v_add_f32 v62, v68, v60
	v_sub_f32 v60, v68, v60
	v_add_f32 v68, v56, v57
	v_sub_f32 v56, v56, v57
	v_add_f32 v57, v58, v55
	v_sub_f32 v55, v58, v55
	v_add_f32 v58, v64, v75
	v_sub_f32 v64, v64, v75
	v_add_f32 v75, v69, v66
	v_sub_f32 v66, v69, v66
	v_add_f32 v69, v67, v65
	v_sub_f32 v65, v67, v65
	v_add_f32 v67, v70, v59
	v_sub_f32 v59, v70, v59
	v_add_f32 v70, v63, v68
	v_sub_f32 v63, v63, v68
	v_add_f32 v68, v62, v57
	v_sub_f32 v57, v62, v57
	v_add_f32 v62, v61, v56
	v_sub_f32 v56, v61, v56
	v_add_f32 v61, v60, v55
	v_sub_f32 v55, v60, v55
	v_mul_f32 v58, v58, v11
	v_mul_f32 v60, v75, v11
	v_mul_f32 v69, v69, v12
	v_mul_f32 v67, v67, v12
	v_mul_f32 v64, v64, v13
	v_mul_f32 v66, v66, v13
	v_mul_f32 v65, v65, v14
	v_mul_f32 v59, v59, v14
	v_mul_f32 v70, v70, v15
	v_mul_f32 v68, v68, v15
	v_mul_f32 v62, v62, v16
	v_mul_f32 v61, v61, v16
	v_mul_f32 v56, v56, v18
	v_mul_f32 v55, v55, v18
	v_mul_f32 v63, v63, v17
	v_mul_f32 v57, v57, v17
	s_nop 0
	v_fma_f32 v75, s19, v67, v58
	v_fma_f32 v76, -s19, v69, v60
	v_fma_f32 v60, s19, v60, v69
	v_fma_f32 v58, -s19, v58, v67
	v_fma_f32 v67, s19, v59, v64
	v_fma_f32 v69, -s19, v65, v66
	v_fma_f32 v65, s19, v66, v65
	v_fma_f32 v59, -s19, v64, v59
	v_fma_f32 v64, s19, v61, v70
	v_fma_f32 v66, -s19, v62, v68
	v_fma_f32 v62, s19, v68, v62
	v_fma_f32 v61, -s19, v70, v61
	v_fma_f32 v68, s19, v55, v63
	v_fma_f32 v70, -s19, v56, v57
	v_fma_f32 v56, s19, v57, v56
	v_fma_f32 v55, -s19, v63, v55
	s_nop 0
	v_fma_f32 v57, s18, v69, v75
	v_fma_f32 v63, -s18, v67, v76
	v_fma_f32 v67, s18, v76, v67
	v_fma_f32 v69, -s18, v75, v69
	v_fma_f32 v75, s18, v59, v60
	v_fma_f32 v76, -s18, v65, v58
	v_fma_f32 v58, s18, v58, v65
	v_fma_f32 v59, -s18, v60, v59
	v_fma_f32 v60, s18, v70, v64
	v_fma_f32 v65, -s18, v68, v66
	v_fma_f32 v66, s18, v66, v68
	v_fma_f32 v64, -s18, v64, v70
	v_fma_f32 v68, s18, v55, v62
	v_fma_f32 v70, -s18, v56, v61
	v_fma_f32 v56, s18, v61, v56
	v_fma_f32 v55, -s18, v62, v55
	s_nop 0
	s_nop 1
	v_permlane32_swap_b32 v57, v67
	v_permlane32_swap_b32 v63, v69
	v_permlane32_swap_b32 v75, v58
	v_permlane32_swap_b32 v76, v59
	s_or_b32 s25, s10, 6
	v_permlane32_swap_b32 v60, v66
	v_permlane32_swap_b32 v65, v64
	v_permlane32_swap_b32 v68, v56
	v_permlane32_swap_b32 v70, v55
	v_permlane16_swap_b32 v57, v75
	v_permlane16_swap_b32 v63, v76
	v_permlane16_swap_b32 v67, v58
	v_permlane16_swap_b32 v69, v59
	s_or_b32 s26, s10, 7
	v_permlane16_swap_b32 v60, v68
	v_permlane16_swap_b32 v65, v70
	v_permlane16_swap_b32 v66, v56
	v_permlane16_swap_b32 v64, v55
	v_fma_f32 v61, s15, v76, v57
	v_fma_f32 v62, -s15, v75, v63
	v_fma_f32 v63, s15, v63, v75
	v_fma_f32 v57, -s15, v57, v76
	v_fma_f32 v75, s15, v59, v67
	v_fma_f32 v76, -s15, v58, v69
	v_fma_f32 v58, s15, v69, v58
	v_fma_f32 v59, -s15, v67, v59
	s_nop 0
	v_fma_f32 v67, s15, v70, v60
	v_fma_f32 v69, -s15, v68, v65
	v_fma_f32 v60, -s15, v60, v70
	v_fma_f32 v70, -s15, v56, v64
	v_fma_f32 v65, s15, v65, v68
	v_fma_f32 v68, s15, v55, v66
	v_fma_f32 v56, s15, v64, v56
	v_fma_f32 v55, -s15, v66, v55
	v_fma_f32 v64, s11, v76, v61
	v_fma_f32 v77, -s11, v75, v62
	v_fma_f32 v75, s11, v62, v75
	v_fma_f32 v61, -s11, v61, v76
	v_fma_f32 v76, s11, v59, v63
	v_fma_f32 v62, -s11, v58, v57
	v_fma_f32 v78, s11, v57, v58
	v_fma_f32 v79, -s11, v63, v59
	s_nop 0
	v_fma_f32 v57, s11, v70, v67
	v_fma_f32 v59, -s11, v68, v69
	v_fma_f32 v69, s11, v69, v68
	v_fma_f32 v70, -s11, v67, v70
	v_fma_f32 v63, s11, v55, v65
	v_readlane_b32 s10, v52, s10
	v_readlane_b32 s20, v52, s24
	v_fma_f32 v80, -s11, v56, v60
	v_fma_f32 v81, s11, v60, v56
	v_fma_f32 v82, -s11, v65, v55
	v_fma_f32 v65, s10, v59, v64
	v_fma_f32 v66, -s10, v57, v77
	v_fma_f32 v58, s10, v77, v57
	v_fma_f32 v59, -s10, v64, v59
	s_nop 0
	v_fma_f32 v67, s10, v80, v76
	v_fma_f32 v68, -s10, v63, v62
	v_fma_f32 v62, s10, v62, v63
	v_fma_f32 v63, -s10, v76, v80
	v_fma_f32 v56, s10, v70, v75
	v_fma_f32 v57, -s10, v69, v61
	v_fma_f32 v55, s10, v61, v69
	v_fma_f32 v64, -s10, v75, v70
	v_fma_f32 v60, s10, v82, v78
	v_fma_f32 v61, -s10, v81, v79
	v_fma_f32 v69, s10, v79, v81
	v_fma_f32 v70, -s10, v78, v82
	s_nop 0
	v_mov_b32_e32 v74, s20
	s_nop 1
	v_mul_f32_dpp v75, v65, v74 row_ror:8 row_mask:0xf bank_mask:0xf
	v_mul_f32_dpp v76, v67, v74 row_ror:8 row_mask:0xf bank_mask:0xf
	v_mul_f32_dpp v77, v56, v74 row_ror:8 row_mask:0xf bank_mask:0xf
	v_mul_f32_dpp v78, v60, v74 row_ror:8 row_mask:0xf bank_mask:0xf
	v_fmac_f32_dpp v65, v66, v74 row_ror:8 row_mask:0xf bank_mask:0xf
	v_fmac_f32_dpp v67, v68, v74 row_ror:8 row_mask:0xf bank_mask:0xf
	v_fmac_f32_dpp v56, v57, v74 row_ror:8 row_mask:0xf bank_mask:0xf
	v_fmac_f32_dpp v60, v61, v74 row_ror:8 row_mask:0xf bank_mask:0xf
	v_sub_f32 v66, v66, v75
	v_sub_f32 v68, v68, v76
	v_sub_f32 v57, v57, v77
	v_sub_f32 v61, v61, v78
	v_readlane_b32 s22, v52, s25
	s_nop 1
	v_mul_f32_dpp v75, v58, v74 row_ror:8 row_mask:0xf bank_mask:0xf
	v_mul_f32_dpp v76, v62, v74 row_ror:8 row_mask:0xf bank_mask:0xf
	v_mul_f32_dpp v77, v55, v74 row_ror:8 row_mask:0xf bank_mask:0xf
	v_mul_f32_dpp v78, v69, v74 row_ror:8 row_mask:0xf bank_mask:0xf
	v_fmac_f32_dpp v58, v59, v74 row_ror:8 row_mask:0xf bank_mask:0xf
	v_fmac_f32_dpp v62, v63, v74 row_ror:8 row_mask:0xf bank_mask:0xf
	v_fmac_f32_dpp v55, v64, v74 row_ror:8 row_mask:0xf bank_mask:0xf
	v_fmac_f32_dpp v69, v70, v74 row_ror:8 row_mask:0xf bank_mask:0xf
	v_sub_f32 v59, v59, v75
	v_sub_f32 v63, v63, v76
	v_sub_f32 v64, v64, v77
	v_sub_f32 v70, v70, v78
	v_readlane_b32 s23, v52, s26
	v_mov_b32_dpp v74, v65 row_half_mirror row_mask:0xf bank_mask:0xf bound_ctrl:1
	v_mov_b32_dpp v75, v67 row_half_mirror row_mask:0xf bank_mask:0xf bound_ctrl:1
	v_mov_b32_dpp v76, v56 row_half_mirror row_mask:0xf bank_mask:0xf bound_ctrl:1
	v_mov_b32_dpp v77, v60 row_half_mirror row_mask:0xf bank_mask:0xf bound_ctrl:1
	v_mov_b32_e32 v73, s22
	v_mov_b32_dpp v78, v66 row_half_mirror row_mask:0xf bank_mask:0xf bound_ctrl:1
	v_mov_b32_dpp v79, v68 row_half_mirror row_mask:0xf bank_mask:0xf bound_ctrl:1
	v_mov_b32_dpp v80, v57 row_half_mirror row_mask:0xf bank_mask:0xf bound_ctrl:1
	v_mov_b32_dpp v81, v61 row_half_mirror row_mask:0xf bank_mask:0xf bound_ctrl:1
	v_mov_b32_dpp v82, v58 row_half_mirror row_mask:0xf bank_mask:0xf bound_ctrl:1
	v_mov_b32_dpp v83, v62 row_half_mirror row_mask:0xf bank_mask:0xf bound_ctrl:1
	v_mov_b32_dpp v84, v55 row_half_mirror row_mask:0xf bank_mask:0xf bound_ctrl:1
	v_mov_b32_dpp v85, v69 row_half_mirror row_mask:0xf bank_mask:0xf bound_ctrl:1
	v_mov_b32_dpp v86, v59 row_half_mirror row_mask:0xf bank_mask:0xf bound_ctrl:1
	v_mov_b32_dpp v87, v63 row_half_mirror row_mask:0xf bank_mask:0xf bound_ctrl:1
	v_mov_b32_dpp v88, v64 row_half_mirror row_mask:0xf bank_mask:0xf bound_ctrl:1
	v_mov_b32_dpp v89, v70 row_half_mirror row_mask:0xf bank_mask:0xf bound_ctrl:1
	v_mul_f32_dpp v90, v74, v73 quad_perm:[3,2,1,0] row_mask:0xf bank_mask:0xf
	v_mul_f32_dpp v91, v75, v73 quad_perm:[3,2,1,0] row_mask:0xf bank_mask:0xf
	v_mul_f32_dpp v92, v76, v73 quad_perm:[3,2,1,0] row_mask:0xf bank_mask:0xf
	v_mul_f32_dpp v93, v77, v73 quad_perm:[3,2,1,0] row_mask:0xf bank_mask:0xf
	v_fmac_f32_dpp v65, v78, v73 quad_perm:[3,2,1,0] row_mask:0xf bank_mask:0xf
	v_fmac_f32_dpp v67, v79, v73 quad_perm:[3,2,1,0] row_mask:0xf bank_mask:0xf
	v_fmac_f32_dpp v56, v80, v73 quad_perm:[3,2,1,0] row_mask:0xf bank_mask:0xf
	v_fmac_f32_dpp v60, v81, v73 quad_perm:[3,2,1,0] row_mask:0xf bank_mask:0xf
	v_sub_f32 v66, v66, v90
	v_sub_f32 v68, v68, v91
	v_sub_f32 v57, v57, v92
	v_sub_f32 v61, v61, v93
	v_mul_f32_dpp v74, v82, v73 quad_perm:[3,2,1,0] row_mask:0xf bank_mask:0xf
	v_mul_f32_dpp v75, v83, v73 quad_perm:[3,2,1,0] row_mask:0xf bank_mask:0xf
	v_mul_f32_dpp v76, v84, v73 quad_perm:[3,2,1,0] row_mask:0xf bank_mask:0xf
	v_mul_f32_dpp v77, v85, v73 quad_perm:[3,2,1,0] row_mask:0xf bank_mask:0xf
	v_fmac_f32_dpp v58, v86, v73 quad_perm:[3,2,1,0] row_mask:0xf bank_mask:0xf
	v_fmac_f32_dpp v62, v87, v73 quad_perm:[3,2,1,0] row_mask:0xf bank_mask:0xf
	v_fmac_f32_dpp v55, v88, v73 quad_perm:[3,2,1,0] row_mask:0xf bank_mask:0xf
	v_fmac_f32_dpp v69, v89, v73 quad_perm:[3,2,1,0] row_mask:0xf bank_mask:0xf
	v_sub_f32 v59, v59, v74
	v_sub_f32 v63, v63, v75
	v_sub_f32 v64, v64, v76
	v_sub_f32 v70, v70, v77
	s_mov_b64 s[8:9], 0
	s_mov_b32 s14, 1
	v_readlane_b32 s21, v52, s21
	s_and_b64 vcc, exec, vcc
	v_mov_b32_e32 v72, s23
	s_nop 1
	v_mul_f32_dpp v73, v65, v72 quad_perm:[2,3,0,1] row_mask:0xf bank_mask:0xf
	v_mul_f32_dpp v74, v67, v72 quad_perm:[2,3,0,1] row_mask:0xf bank_mask:0xf
	v_mul_f32_dpp v75, v56, v72 quad_perm:[2,3,0,1] row_mask:0xf bank_mask:0xf
	v_mul_f32_dpp v76, v60, v72 quad_perm:[2,3,0,1] row_mask:0xf bank_mask:0xf
	v_fmac_f32_dpp v65, v66, v72 quad_perm:[2,3,0,1] row_mask:0xf bank_mask:0xf
	v_fmac_f32_dpp v67, v68, v72 quad_perm:[2,3,0,1] row_mask:0xf bank_mask:0xf
	v_fmac_f32_dpp v56, v57, v72 quad_perm:[2,3,0,1] row_mask:0xf bank_mask:0xf
	v_fmac_f32_dpp v60, v61, v72 quad_perm:[2,3,0,1] row_mask:0xf bank_mask:0xf
	v_sub_f32 v66, v66, v73
	v_sub_f32 v68, v68, v74
	v_sub_f32 v57, v57, v75
	v_sub_f32 v61, v61, v76
	v_mov_b32_e32 v71, s21
	v_mul_f32_dpp v73, v58, v72 quad_perm:[2,3,0,1] row_mask:0xf bank_mask:0xf
	v_mul_f32_dpp v74, v62, v72 quad_perm:[2,3,0,1] row_mask:0xf bank_mask:0xf
	v_mul_f32_dpp v75, v55, v72 quad_perm:[2,3,0,1] row_mask:0xf bank_mask:0xf
	v_mul_f32_dpp v76, v69, v72 quad_perm:[2,3,0,1] row_mask:0xf bank_mask:0xf
	v_fmac_f32_dpp v58, v59, v72 quad_perm:[2,3,0,1] row_mask:0xf bank_mask:0xf
	v_fmac_f32_dpp v62, v63, v72 quad_perm:[2,3,0,1] row_mask:0xf bank_mask:0xf
	v_fmac_f32_dpp v55, v64, v72 quad_perm:[2,3,0,1] row_mask:0xf bank_mask:0xf
	v_fmac_f32_dpp v69, v70, v72 quad_perm:[2,3,0,1] row_mask:0xf bank_mask:0xf
	v_sub_f32 v59, v59, v73
	v_sub_f32 v63, v63, v74
	v_sub_f32 v64, v64, v75
	v_sub_f32 v70, v70, v76
	s_nop 0
	s_nop 1
	v_mul_f32_dpp v72, v65, v71 quad_perm:[1,0,3,2] row_mask:0xf bank_mask:0xf
	v_mul_f32_dpp v73, v67, v71 quad_perm:[1,0,3,2] row_mask:0xf bank_mask:0xf
	v_mul_f32_dpp v74, v56, v71 quad_perm:[1,0,3,2] row_mask:0xf bank_mask:0xf
	v_mul_f32_dpp v75, v60, v71 quad_perm:[1,0,3,2] row_mask:0xf bank_mask:0xf
	v_fmac_f32_dpp v65, v66, v71 quad_perm:[1,0,3,2] row_mask:0xf bank_mask:0xf
	v_fmac_f32_dpp v67, v68, v71 quad_perm:[1,0,3,2] row_mask:0xf bank_mask:0xf
	v_fmac_f32_dpp v56, v57, v71 quad_perm:[1,0,3,2] row_mask:0xf bank_mask:0xf
	v_fmac_f32_dpp v60, v61, v71 quad_perm:[1,0,3,2] row_mask:0xf bank_mask:0xf
	v_sub_f32 v66, v66, v72
	v_sub_f32 v68, v68, v73
	v_sub_f32 v57, v57, v74
	v_sub_f32 v61, v61, v75
	s_nop 0
	s_nop 1
	v_mul_f32_dpp v72, v58, v71 quad_perm:[1,0,3,2] row_mask:0xf bank_mask:0xf
	v_mul_f32_dpp v73, v62, v71 quad_perm:[1,0,3,2] row_mask:0xf bank_mask:0xf
	v_mul_f32_dpp v74, v55, v71 quad_perm:[1,0,3,2] row_mask:0xf bank_mask:0xf
	v_mul_f32_dpp v75, v69, v71 quad_perm:[1,0,3,2] row_mask:0xf bank_mask:0xf
	v_fmac_f32_dpp v58, v59, v71 quad_perm:[1,0,3,2] row_mask:0xf bank_mask:0xf
	v_fmac_f32_dpp v62, v63, v71 quad_perm:[1,0,3,2] row_mask:0xf bank_mask:0xf
	v_fmac_f32_dpp v55, v64, v71 quad_perm:[1,0,3,2] row_mask:0xf bank_mask:0xf
	v_fmac_f32_dpp v69, v70, v71 quad_perm:[1,0,3,2] row_mask:0xf bank_mask:0xf
	v_sub_f32 v59, v59, v72
	v_sub_f32 v63, v63, v73
	v_sub_f32 v64, v64, v74
	v_sub_f32 v70, v70, v75
	s_cbranch_vccz .LBB0_24
	v_mul_f32_e32 v2, v53, v54
	v_mul_f32 v3, v65, v2
	v_mul_f32 v55, v57, v2
	v_mul_f32 v4, v66, v2
	v_mul_f32 v52, v67, v2
	v_mul_f32 v53, v68, v2
	v_mul_f32 v54, v56, v2
	v_mul_f32 v57, v3, v3
	v_mul_f32 v56, v60, v2
	v_mul_f32 v2, v61, v2
	s_mov_b64 s[10:11], 0
	v_fma_f32 v57, v4, v4, v57
	s_nop 0
	v_fma_f32 v57, v52, v52, v57
	s_nop 0
	v_fma_f32 v57, v53, v53, v57
	s_nop 0
	v_fma_f32 v57, v54, v54, v57
	s_nop 0
	v_fma_f32 v57, v55, v55, v57
	s_nop 0
	v_fma_f32 v57, v56, v56, v57
	s_nop 0
	v_fma_f32 v57, v2, v2, v57
	s_nop 1
	v_add_f32_dpp v57, v57, v57 quad_perm:[1,0,3,2] row_mask:0xf bank_mask:0xf bound_ctrl:1
	s_nop 1
	v_add_f32_dpp v57, v57, v57 quad_perm:[2,3,0,1] row_mask:0xf bank_mask:0xf bound_ctrl:1
	s_waitcnt lgkmcnt(0)
	s_nop 1
	v_add_f32_dpp v57, v57, v57 row_half_mirror row_mask:0xf bank_mask:0xf bound_ctrl:1
	s_nop 1
	v_add_f32_dpp v57, v57, v57 row_ror:8 row_mask:0xf bank_mask:0xf bound_ctrl:1
	v_mov_b32_e32 v58, v57
	s_nop 1
	v_permlane16_swap_b32 v58, v57
	s_waitcnt lgkmcnt(0)
	v_add_f32_e32 v57, v57, v58
	ds_bpermute_b32 v58, v19, v57
	s_waitcnt lgkmcnt(0)
	v_add_f32_e32 v57, v57, v58
	v_mul_f32_e32 v58, 0x4f800000, v57
	v_cmp_gt_f32_e32 vcc, s17, v57
	s_nop 1
	v_cndmask_b32_e32 v57, v57, v58, vcc
	v_sqrt_f32_e32 v58, v57
	s_nop 0
	v_add_u32_e32 v59, -1, v58
	v_add_u32_e32 v60, 1, v58
	v_fma_f32 v61, -v59, v58, v57
	v_fma_f32 v62, -v60, v58, v57
	v_cmp_ge_f32_e64 s[8:9], 0, v61
	s_nop 1
	v_cndmask_b32_e64 v58, v58, v59, s[8:9]
	v_cmp_lt_f32_e64 s[8:9], 0, v62
	s_nop 1
	v_cndmask_b32_e64 v58, v58, v60, s[8:9]
	v_mul_f32_e32 v59, 0x37800000, v58
	v_cndmask_b32_e32 v58, v58, v59, vcc
	v_cmp_class_f32_e32 vcc, v57, v41
	s_nop 1
	v_cndmask_b32_e32 v57, v58, v57, vcc
	v_add_f32_e32 v57, 0x322bcc77, v57
	v_div_scale_f32 v58, s[8:9], v57, v57, 1.0
	v_rcp_f32_e32 v59, v58
	v_div_scale_f32 v60, vcc, 1.0, v57, 1.0
	v_fma_f32 v61, -v58, v59, 1.0
	v_fmac_f32_e32 v59, v61, v59
	v_mul_f32_e32 v61, v60, v59
	v_fma_f32 v62, -v58, v61, v60
	v_fmac_f32_e32 v61, v62, v59
	v_fma_f32 v58, -v58, v61, v60
	v_div_fmas_f32 v58, v58, v59, v61
	v_div_fixup_f32 v57, v58, v57, 1.0
	v_mul_f32 v3, v3, v57
	v_mul_f32 v4, v4, v57
	v_mul_f32 v52, v52, v57
	v_mul_f32 v53, v53, v57
	v_mul_f32 v2, v2, v57
	s_nop 0
	v_mul_f32 v58, v3, v42
	s_nop 0
	v_max_f32 v3, v3, v58
	v_mul_f32 v58, v4, v42
	s_nop 0
	v_max_f32 v4, v4, v58
	v_mul_f32 v58, v52, v42
	s_nop 0
	v_max_f32 v52, v52, v58
	v_mul_f32 v58, v53, v42
	s_nop 0
	v_max_f32 v58, v53, v58
	v_mul_f32 v53, v54, v57
	v_mul_f32 v54, v55, v57
	s_nop 0
	v_mul_f32 v55, v53, v42
	s_nop 0
	v_max_f32 v55, v53, v55
	v_mul_f32 v53, v54, v42
	s_nop 0
	v_max_f32 v59, v54, v53
	v_mul_f32 v53, v56, v57
	s_nop 0
	v_mul_f32 v54, v53, v42
	s_nop 0
	v_max_f32 v60, v53, v54
	v_mul_f32 v53, v2, v42
	s_nop 0
	v_max_f32 v2, v2, v53
	v_mul_f32 v53, v3, v3
	s_nop 0
	v_fma_f32 v53, v4, v4, v53
	s_nop 0
	v_fma_f32 v53, v52, v52, v53
	s_nop 0
	v_fma_f32 v53, v58, v58, v53
	s_nop 0
	v_fma_f32 v53, v55, v55, v53
	s_nop 0
	v_fma_f32 v53, v59, v59, v53
	s_nop 0
	v_fma_f32 v53, v60, v60, v53
	s_nop 0
	v_fma_f32 v53, v2, v2, v53
	s_nop 1
	v_add_f32_dpp v53, v53, v53 quad_perm:[1,0,3,2] row_mask:0xf bank_mask:0xf bound_ctrl:1
	s_nop 1
	v_add_f32_dpp v53, v53, v53 quad_perm:[2,3,0,1] row_mask:0xf bank_mask:0xf bound_ctrl:1
	s_waitcnt lgkmcnt(0)
	s_nop 1
	v_add_f32_dpp v53, v53, v53 row_half_mirror row_mask:0xf bank_mask:0xf bound_ctrl:1
	s_nop 1
	v_add_f32_dpp v53, v53, v53 row_ror:8 row_mask:0xf bank_mask:0xf bound_ctrl:1
	v_mov_b32_e32 v54, v53
	s_nop 1
	v_permlane16_swap_b32 v54, v53
	s_waitcnt lgkmcnt(0)
	v_add_f32_e32 v53, v53, v54
	ds_bpermute_b32 v54, v19, v53
	s_waitcnt lgkmcnt(0)
	v_add_f32_e32 v53, v53, v54
	v_mul_f32_e32 v54, 0x4f800000, v53
	v_cmp_gt_f32_e32 vcc, s17, v53
	s_nop 1
	v_cndmask_b32_e32 v53, v53, v54, vcc
	v_sqrt_f32_e32 v54, v53
	s_nop 0
	v_add_u32_e32 v56, -1, v54
	v_fma_f32 v57, -v56, v54, v53
	v_cmp_ge_f32_e64 s[8:9], 0, v57
	v_add_u32_e32 v57, 1, v54
	s_nop 0
	v_cndmask_b32_e64 v56, v54, v56, s[8:9]
	v_fma_f32 v54, -v57, v54, v53
	v_cmp_lt_f32_e64 s[8:9], 0, v54
	s_nop 1
	v_cndmask_b32_e64 v54, v56, v57, s[8:9]
	v_mul_f32_e32 v56, 0x37800000, v54
	v_cndmask_b32_e32 v54, v54, v56, vcc
	v_cmp_class_f32_e32 vcc, v53, v41
	s_nop 1
	v_cndmask_b32_e32 v53, v54, v53, vcc
	v_div_scale_f32 v54, s[8:9], v53, v53, 1.0
	v_rcp_f32_e32 v56, v54
	s_nop 0
	v_fma_f32 v57, -v54, v56, 1.0
	v_fmac_f32_e32 v56, v57, v56
	v_div_scale_f32 v57, vcc, 1.0, v53, 1.0
	v_mul_f32_e32 v61, v57, v56
	v_fma_f32 v62, -v54, v61, v57
	v_fmac_f32_e32 v61, v62, v56
	v_fma_f32 v54, -v54, v61, v57
	v_div_fmas_f32 v54, v54, v56, v61
	v_div_fixup_f32 v61, v54, v53, 1.0
	v_mul_f32 v54, v3, v61
	v_mul_f32 v3, v4, v61
	v_mul_f32 v53, v52, v61
	v_mul_f32 v57, v58, v61
	v_mul_f32 v52, v55, v61
	v_mul_f32 v56, v59, v61
	v_mul_f32 v55, v60, v61
	v_mul_f32 v58, v2, v61
	s_branch .LBB0_11
